# differential attention second-pass epilogue: the 64 per-lane O1 re-reads issued together and waited once (were 16 dependent load-wait rounds)
# speedup vs baseline: 1.0015x; 1.0015x over previous
.LBB0_493:
	s_or_b64 exec, exec, s[2:3]
	v_mov_b64_e32 v[80:81], s[34:35]
	v_lshlrev_b32_e32 v160, 11, v204
	v_mad_u64_u32 v[80:81], s[2:3], v204, s76, v[80:81]
	v_lshl_add_u64 v[82:83], s[74:75], 0, v[160:161]
	v_lshlrev_b32_e32 v160, 1, v203
	v_lshl_add_u64 v[82:83], v[82:83], 0, v[160:161]
	v_lshl_add_u64 v[80:81], v[80:81], 0, v[160:161]
	v_lshlrev_b32_e32 v160, 13, v202
	s_waitcnt lgkmcnt(0)
	v_add_u32_e32 v64, v64, v190
	s_mov_b32 s6, s72
	v_lshl_add_u64 v[84:85], v[82:83], 0, v[160:161]
	ds_read_b128 v[76:79], v64
	ds_read_b128 v[72:75], v64 offset:32
	ds_read_b128 v[68:71], v64 offset:64
	ds_read_b128 v[64:67], v64 offset:96
	global_load_ushort v128, v[84:85], off
	global_load_ushort v129, v[84:85], off offset:64
	global_load_ushort v130, v[84:85], off offset:128
	global_load_ushort v131, v[84:85], off offset:192
	global_load_ushort v132, v[84:85], off offset:2048
	global_load_ushort v133, v[84:85], off offset:2112
	global_load_ushort v134, v[84:85], off offset:2176
	global_load_ushort v135, v[84:85], off offset:2240
	s_mov_b64 s[2:3], 0x1000
	v_lshl_add_u64 v[214:215], v[84:85], 0, s[2:3]
	global_load_ushort v136, v[214:215], off
	global_load_ushort v137, v[214:215], off offset:64
	global_load_ushort v138, v[214:215], off offset:128
	global_load_ushort v139, v[214:215], off offset:192
	global_load_ushort v140, v[214:215], off offset:2048
	global_load_ushort v141, v[214:215], off offset:2112
	global_load_ushort v142, v[214:215], off offset:2176
	global_load_ushort v143, v[214:215], off offset:2240
	s_mov_b64 s[2:3], 0x4000
	v_lshl_add_u64 v[214:215], v[84:85], 0, s[2:3]
	global_load_ushort v162, v[214:215], off
	global_load_ushort v163, v[214:215], off offset:64
	global_load_ushort v164, v[214:215], off offset:128
	global_load_ushort v165, v[214:215], off offset:192
	global_load_ushort v166, v[214:215], off offset:2048
	global_load_ushort v167, v[214:215], off offset:2112
	global_load_ushort v168, v[214:215], off offset:2176
	global_load_ushort v169, v[214:215], off offset:2240
	s_mov_b64 s[2:3], 0x5000
	v_lshl_add_u64 v[214:215], v[84:85], 0, s[2:3]
	global_load_ushort v170, v[214:215], off
	global_load_ushort v171, v[214:215], off offset:64
	global_load_ushort v172, v[214:215], off offset:128
	global_load_ushort v173, v[214:215], off offset:192
	global_load_ushort v174, v[214:215], off offset:2048
	global_load_ushort v175, v[214:215], off offset:2112
	global_load_ushort v176, v[214:215], off offset:2176
	global_load_ushort v177, v[214:215], off offset:2240
	s_mov_b64 s[2:3], 0x8000
	v_lshl_add_u64 v[214:215], v[84:85], 0, s[2:3]
	global_load_ushort v178, v[214:215], off
	global_load_ushort v179, v[214:215], off offset:64
	global_load_ushort v180, v[214:215], off offset:128
	global_load_ushort v181, v[214:215], off offset:192
	global_load_ushort v182, v[214:215], off offset:2048
	global_load_ushort v183, v[214:215], off offset:2112
	global_load_ushort v184, v[214:215], off offset:2176
	global_load_ushort v185, v[214:215], off offset:2240
	s_mov_b64 s[2:3], 0x9000
	v_lshl_add_u64 v[214:215], v[84:85], 0, s[2:3]
	global_load_ushort v186, v[214:215], off
	global_load_ushort v187, v[214:215], off offset:64
	global_load_ushort v188, v[214:215], off offset:128
	global_load_ushort v189, v[214:215], off offset:192
	global_load_ushort v191, v[214:215], off offset:2048
	global_load_ushort v192, v[214:215], off offset:2112
	global_load_ushort v193, v[214:215], off offset:2176
	global_load_ushort v194, v[214:215], off offset:2240
	s_mov_b64 s[2:3], 0xc000
	v_lshl_add_u64 v[214:215], v[84:85], 0, s[2:3]
	global_load_ushort v195, v[214:215], off
	global_load_ushort v196, v[214:215], off offset:64
	global_load_ushort v197, v[214:215], off offset:128
	global_load_ushort v198, v[214:215], off offset:192
	global_load_ushort v199, v[214:215], off offset:2048
	global_load_ushort v200, v[214:215], off offset:2112
	global_load_ushort v201, v[214:215], off offset:2176
	global_load_ushort v205, v[214:215], off offset:2240
	s_mov_b64 s[2:3], 0xd000
	v_lshl_add_u64 v[214:215], v[84:85], 0, s[2:3]
	global_load_ushort v206, v[214:215], off
	global_load_ushort v207, v[214:215], off offset:64
	global_load_ushort v208, v[214:215], off offset:128
	global_load_ushort v209, v[214:215], off offset:192
	global_load_ushort v210, v[214:215], off offset:2048
	global_load_ushort v211, v[214:215], off offset:2112
	global_load_ushort v212, v[214:215], off offset:2176
	global_load_ushort v213, v[214:215], off offset:2240
	v_readlane_b32 s2, v255, 42
	v_readlane_b32 s3, v255, 43
	s_add_u32 s2, s18, s2
	v_lshlrev_b32_e32 v85, 2, v203
	s_addc_u32 s3, s19, s3
	s_nop 1
	global_load_dword v89, v85, s[2:3]
	global_load_dword v90, v85, s[2:3] offset:128
	global_load_dword v91, v85, s[2:3] offset:256
	global_load_dword v92, v85, s[2:3] offset:384
	s_waitcnt lgkmcnt(3)
	v_rcp_f32_e32 v76, v76
	s_cmp_eq_u32 s6, 0
	s_cselect_b64 vcc, -1, 0
	v_rcp_f32_e32 v77, v77
	v_mul_f32_e32 v16, v16, v76
	v_mul_f32_e32 v0, v0, v76
	v_mul_f32_e32 v32, v32, v76
	v_mul_f32_e32 v48, v48, v76
	v_mul_f32_e32 v1, v1, v77
	v_mul_f32_e32 v17, v17, v77
	v_mul_f32_e32 v33, v33, v77
	v_mul_f32_e32 v49, v49, v77
	s_mov_b64 s[2:3], 0x1a00
	s_addk_i32 s81, 0x1000
	s_waitcnt vmcnt(0)
	v_mov_b32_e32 v86, v128
	v_mov_b32_e32 v87, v129
	v_mov_b32_e32 v88, v130
	v_mov_b32_e32 v84, v131
	v_lshlrev_b32_e32 v76, 16, v86
	v_lshlrev_b32_e32 v85, 16, v87
	v_fma_f32 v93, -s78, v16, v85
	v_lshlrev_b32_e32 v86, 16, v88
	v_fma_f32 v88, -s78, v0, v76
	v_mul_f32_e32 v0, v93, v93
	v_lshlrev_b32_e32 v84, 16, v84
	v_fma_f32 v94, -s78, v32, v86
	v_fmac_f32_e32 v0, v88, v88
	v_fma_f32 v95, -s78, v48, v84
	v_fmac_f32_e32 v0, v94, v94
	v_fmac_f32_e32 v0, v95, v95
	ds_swizzle_b32 v16, v0 offset:swizzle(SWAP,1)
	v_mov_b32_e32 v76, 0x3f4ccccd
	v_mul_u32_u24_e32 v84, 0x6800, v202
	v_mov_b32_e32 v85, v161
	v_mov_b32_e32 v87, v161
	s_waitcnt lgkmcnt(0)
	v_add_f32_e32 v0, v0, v16
	ds_swizzle_b32 v16, v0 offset:swizzle(SWAP,2)
	v_lshl_add_u64 v[84:85], v[80:81], 0, v[84:85]
	s_waitcnt lgkmcnt(0)
	v_add_f32_e32 v0, v0, v16
	ds_swizzle_b32 v16, v0 offset:swizzle(SWAP,4)
	s_waitcnt lgkmcnt(0)
	v_add_f32_e32 v16, v0, v16
	ds_swizzle_b32 v32, v16 offset:swizzle(SWAP,8)
	v_lshl_or_b32 v0, v202, 2, 1
	v_lshlrev_b32_e32 v86, 11, v0
	v_lshl_add_u64 v[86:87], v[82:83], 0, v[86:87]
	s_waitcnt lgkmcnt(0)
	v_add_f32_e32 v32, v16, v32
	ds_swizzle_b32 v48, v32 offset:swizzle(SWAP,16)
	v_mov_b32_e32 v16, 0x3f24fd5c
	v_cndmask_b32_e32 v76, v16, v76, vcc
	s_waitcnt vmcnt(3)
	v_mul_f32_e32 v16, v89, v76
	s_waitcnt lgkmcnt(0)
	v_add_f32_e32 v32, v32, v48
	v_fmamk_f32 v32, v32, 0x3c000000, v240
	v_rsq_f32_e32 v89, v32
	s_waitcnt vmcnt(2)
	v_mul_f32_e32 v32, v76, v90
	s_waitcnt vmcnt(1)
	v_mul_f32_e32 v48, v76, v91
	s_waitcnt vmcnt(0)
	v_mul_f32_e32 v76, v76, v92
	v_mul_f32_e32 v88, v88, v89
	v_mul_f32_e32 v90, v93, v89
	v_mul_f32_e32 v91, v94, v89
	v_mul_f32_e32 v89, v95, v89
	v_mul_f32_e32 v88, v16, v88
	v_mul_f32_e32 v90, v32, v90
	v_mul_f32_e32 v91, v48, v91
	v_mul_f32_e32 v89, v76, v89
	v_cvt_pk_bf16_f32 v88, v88, s0
	v_cvt_pk_bf16_f32 v90, v90, s0
	v_cvt_pk_bf16_f32 v91, v91, s0
	v_cvt_pk_bf16_f32 v89, v89, s0
	global_store_short v[84:85], v88, off
	global_store_short v[84:85], v90, off offset:64
	global_store_short v[84:85], v91, off offset:128
	global_store_short v[84:85], v89, off offset:192
	v_mov_b32_e32 v84, v132
	s_nop 0
	v_mov_b32_e32 v85, v133
	v_mov_b32_e32 v88, v134
	s_nop 0
	v_mov_b32_e32 v86, v135
	v_mov_b32_e32 v87, v161
	v_lshlrev_b32_e32 v77, 16, v84
	v_lshlrev_b32_e32 v84, 16, v85
	v_fma_f32 v17, -s78, v17, v84
	v_lshlrev_b32_e32 v85, 16, v88
	v_fma_f32 v1, -s78, v1, v77
	v_mul_f32_e32 v77, v17, v17
	v_lshlrev_b32_e32 v86, 16, v86
	v_fma_f32 v33, -s78, v33, v85
	v_fmac_f32_e32 v77, v1, v1
	v_fma_f32 v49, -s78, v49, v86
	v_fmac_f32_e32 v77, v33, v33
	v_fmac_f32_e32 v77, v49, v49
	ds_swizzle_b32 v84, v77 offset:swizzle(SWAP,1)
	v_mov_b32_e32 v85, v161
	s_waitcnt lgkmcnt(0)
	v_add_f32_e32 v77, v77, v84
	ds_swizzle_b32 v84, v77 offset:swizzle(SWAP,2)
	s_waitcnt lgkmcnt(0)
	v_add_f32_e32 v77, v77, v84
	ds_swizzle_b32 v84, v77 offset:swizzle(SWAP,4)
	s_waitcnt lgkmcnt(0)
	v_add_f32_e32 v77, v77, v84
	ds_swizzle_b32 v84, v77 offset:swizzle(SWAP,8)
	s_waitcnt lgkmcnt(0)
	v_add_f32_e32 v77, v77, v84
	ds_swizzle_b32 v86, v77 offset:swizzle(SWAP,16)
	v_mul_u32_u24_e32 v84, 0x1a00, v0
	v_lshl_add_u64 v[84:85], v[80:81], 0, v[84:85]
	v_lshl_add_u64 v[88:89], v[84:85], 0, s[2:3]
	s_movk_i32 s2, 0x1000
	s_waitcnt lgkmcnt(0)
	v_add_f32_e32 v77, v77, v86
	v_fmamk_f32 v77, v77, 0x3c000000, v240
	v_rsq_f32_e32 v77, v77
	v_or_b32_e32 v86, 0x1000, v160
	v_lshl_add_u64 v[86:87], v[82:83], 0, v[86:87]
	v_mul_f32_e32 v1, v1, v77
	v_mul_f32_e32 v17, v17, v77
	v_mul_f32_e32 v33, v33, v77
	v_mul_f32_e32 v49, v49, v77
	v_mul_f32_e32 v1, v16, v1
	v_mul_f32_e32 v17, v32, v17
	v_mul_f32_e32 v33, v48, v33
	v_mul_f32_e32 v49, v76, v49
	v_cvt_pk_bf16_f32 v1, v1, s0
	v_cvt_pk_bf16_f32 v17, v17, s0
	v_cvt_pk_bf16_f32 v33, v33, s0
	v_cvt_pk_bf16_f32 v49, v49, s0
	global_store_short v[84:85], v1, off
	global_store_short v[84:85], v17, off offset:64
	global_store_short v[84:85], v33, off offset:128
	global_store_short v[84:85], v49, off offset:192
	v_mov_b32_e32 v1, v136
	s_nop 0
	v_mov_b32_e32 v17, v137
	v_mov_b32_e32 v33, v138
	v_mov_b32_e32 v49, v139
	v_rcp_f32_e32 v77, v78
	v_add_co_u32_e32 v84, vcc, s2, v84
	v_mov_b32_e32 v87, v161
	v_mul_f32_e32 v2, v2, v77
	v_mul_f32_e32 v18, v18, v77
	v_mul_f32_e32 v34, v34, v77
	v_mul_f32_e32 v50, v50, v77
	v_or_b32_e32 v86, 0x1800, v160
	v_addc_co_u32_e32 v85, vcc, 0, v85, vcc
	v_lshl_add_u64 v[86:87], v[82:83], 0, v[86:87]
	s_add_i32 s2, s86, 0x100
	s_cmpk_gt_i32 s86, 0xff
	s_mov_b32 s86, s2
	v_lshlrev_b32_e32 v1, 16, v1
	v_lshlrev_b32_e32 v17, 16, v17
	v_lshlrev_b32_e32 v33, 16, v33
	v_fma_f32 v1, -s78, v2, v1
	v_fma_f32 v2, -s78, v18, v17
	v_fma_f32 v17, -s78, v34, v33
	v_mul_f32_e32 v33, v2, v2
	v_lshlrev_b32_e32 v49, 16, v49
	v_fmac_f32_e32 v33, v1, v1
	v_fma_f32 v18, -s78, v50, v49
	v_fmac_f32_e32 v33, v17, v17
	v_fmac_f32_e32 v33, v18, v18
	ds_swizzle_b32 v34, v33 offset:swizzle(SWAP,1)
	s_waitcnt lgkmcnt(0)
	v_add_f32_e32 v33, v33, v34
	ds_swizzle_b32 v34, v33 offset:swizzle(SWAP,2)
	s_waitcnt lgkmcnt(0)
	v_add_f32_e32 v33, v33, v34
	ds_swizzle_b32 v34, v33 offset:swizzle(SWAP,4)
	s_waitcnt lgkmcnt(0)
	v_add_f32_e32 v33, v33, v34
	ds_swizzle_b32 v34, v33 offset:swizzle(SWAP,8)
	s_waitcnt lgkmcnt(0)
	v_add_f32_e32 v33, v33, v34
	ds_swizzle_b32 v34, v33 offset:swizzle(SWAP,16)
	s_waitcnt lgkmcnt(0)
	v_add_f32_e32 v33, v33, v34
	v_fmamk_f32 v33, v33, 0x3c000000, v240
	v_rsq_f32_e32 v33, v33
	s_nop 0
	v_mul_f32_e32 v1, v1, v33
	v_mul_f32_e32 v2, v2, v33
	v_mul_f32_e32 v17, v17, v33
	v_mul_f32_e32 v18, v18, v33
	v_mul_f32_e32 v1, v16, v1
	v_mul_f32_e32 v2, v32, v2
	v_mul_f32_e32 v17, v48, v17
	v_mul_f32_e32 v18, v76, v18
	v_cvt_pk_bf16_f32 v1, v1, s0
	v_cvt_pk_bf16_f32 v2, v2, s0
	v_cvt_pk_bf16_f32 v17, v17, s0
	v_cvt_pk_bf16_f32 v18, v18, s0
	global_store_short v[84:85], v1, off offset:2560
	global_store_short v[88:89], v2, off offset:64
	global_store_short v[88:89], v17, off offset:128
	global_store_short v[88:89], v18, off offset:192
	v_mov_b32_e32 v1, v140
	s_nop 0
	v_mov_b32_e32 v2, v141
	v_mov_b32_e32 v17, v142
	v_mov_b32_e32 v18, v143
	v_rcp_f32_e32 v33, v79
	v_lshlrev_b32_e32 v1, 16, v1
	v_mul_f32_e32 v19, v19, v33
	v_lshlrev_b32_e32 v2, 16, v2
	v_mul_f32_e32 v3, v3, v33
	v_mul_f32_e32 v34, v35, v33
	v_fma_f32 v35, -s78, v19, v2
	v_lshlrev_b32_e32 v17, 16, v17
	v_fma_f32 v1, -s78, v3, v1
	v_mul_f32_e32 v2, v35, v35
	v_mul_f32_e32 v33, v51, v33
	v_lshlrev_b32_e32 v18, 16, v18
	v_fma_f32 v17, -s78, v34, v17
	v_fmac_f32_e32 v2, v1, v1
	v_fma_f32 v33, -s78, v33, v18
	v_fmac_f32_e32 v2, v17, v17
	v_fmac_f32_e32 v2, v33, v33
	ds_swizzle_b32 v3, v2 offset:swizzle(SWAP,1)
	v_mov_b32_e32 v19, v161
	s_waitcnt lgkmcnt(0)
	v_add_f32_e32 v2, v2, v3
	ds_swizzle_b32 v3, v2 offset:swizzle(SWAP,2)
	s_waitcnt lgkmcnt(0)
	v_add_f32_e32 v2, v2, v3
	ds_swizzle_b32 v3, v2 offset:swizzle(SWAP,4)
	s_waitcnt lgkmcnt(0)
	v_add_f32_e32 v2, v2, v3
	ds_swizzle_b32 v3, v2 offset:swizzle(SWAP,8)
	s_waitcnt lgkmcnt(0)
	v_add_f32_e32 v18, v2, v3
	ds_swizzle_b32 v34, v18 offset:swizzle(SWAP,16)
	v_mov_b32_e32 v2, 0x3400
	v_mov_b32_e32 v3, v161
	v_mad_u32_u24 v2, v0, s76, v2
	v_lshl_add_u64 v[2:3], v[80:81], 0, v[2:3]
	s_waitcnt lgkmcnt(0)
	v_add_f32_e32 v18, v18, v34
	v_fmamk_f32 v18, v18, 0x3c000000, v240
	v_rsq_f32_e32 v34, v18
	v_or_b32_e32 v18, 0x4000, v160
	v_lshl_add_u64 v[18:19], v[82:83], 0, v[18:19]
	v_mul_f32_e32 v1, v1, v34
	v_mul_f32_e32 v35, v35, v34
	v_mul_f32_e32 v17, v17, v34
	v_mul_f32_e32 v33, v33, v34
	v_mul_f32_e32 v1, v16, v1
	v_mul_f32_e32 v34, v32, v35
	v_mul_f32_e32 v17, v48, v17
	v_mul_f32_e32 v33, v76, v33
	v_cvt_pk_bf16_f32 v1, v1, s0
	v_cvt_pk_bf16_f32 v34, v34, s0
	v_cvt_pk_bf16_f32 v17, v17, s0
	v_cvt_pk_bf16_f32 v33, v33, s0
	global_store_short v[2:3], v1, off
	global_store_short v[2:3], v34, off offset:64
	global_store_short v[2:3], v17, off offset:128
	global_store_short v[2:3], v33, off offset:192
	v_mov_b32_e32 v1, v162
	s_nop 0
	v_mov_b32_e32 v2, v163
	v_mov_b32_e32 v3, v164
	v_mov_b32_e32 v17, v165
	v_rcp_f32_e32 v18, v72
	v_lshlrev_b32_e32 v1, 16, v1
	v_mul_f32_e32 v4, v4, v18
	v_mul_f32_e32 v19, v20, v18
	v_lshlrev_b32_e32 v2, 16, v2
	v_fma_f32 v1, -s78, v4, v1
	v_fma_f32 v4, -s78, v19, v2
	v_mul_f32_e32 v20, v36, v18
	v_lshlrev_b32_e32 v3, 16, v3
	v_mul_f32_e32 v2, v4, v4
	v_mul_f32_e32 v18, v52, v18
	v_lshlrev_b32_e32 v17, 16, v17
	v_fma_f32 v20, -s78, v20, v3
	v_fmac_f32_e32 v2, v1, v1
	v_fma_f32 v17, -s78, v18, v17
	v_fmac_f32_e32 v2, v20, v20
	v_fmac_f32_e32 v2, v17, v17
	ds_swizzle_b32 v3, v2 offset:swizzle(SWAP,1)
	v_mov_b32_e32 v19, v161
	s_waitcnt lgkmcnt(0)
	v_add_f32_e32 v2, v2, v3
	ds_swizzle_b32 v3, v2 offset:swizzle(SWAP,2)
	s_waitcnt lgkmcnt(0)
	v_add_f32_e32 v2, v2, v3
	ds_swizzle_b32 v3, v2 offset:swizzle(SWAP,4)
	s_waitcnt lgkmcnt(0)
	v_add_f32_e32 v2, v2, v3
	ds_swizzle_b32 v3, v2 offset:swizzle(SWAP,8)
	s_waitcnt lgkmcnt(0)
	v_add_f32_e32 v18, v2, v3
	ds_swizzle_b32 v33, v18 offset:swizzle(SWAP,16)
	v_mov_b32_e32 v2, 0xb600
	v_mov_b32_e32 v3, v161
	v_mad_u32_u24 v2, v0, s76, v2
	v_lshl_add_u64 v[2:3], v[80:81], 0, v[2:3]
	s_waitcnt lgkmcnt(0)
	v_add_f32_e32 v18, v18, v33
	v_fmamk_f32 v18, v18, 0x3c000000, v240
	v_rsq_f32_e32 v33, v18
	v_or_b32_e32 v18, 0x4800, v160
	v_lshl_add_u64 v[18:19], v[82:83], 0, v[18:19]
	v_mul_f32_e32 v1, v1, v33
	v_mul_f32_e32 v4, v4, v33
	v_mul_f32_e32 v20, v20, v33
	v_mul_f32_e32 v17, v17, v33
	v_mul_f32_e32 v1, v16, v1
	v_mul_f32_e32 v4, v32, v4
	v_mul_f32_e32 v20, v48, v20
	v_mul_f32_e32 v17, v76, v17
	v_cvt_pk_bf16_f32 v1, v1, s0
	v_cvt_pk_bf16_f32 v4, v4, s0
	v_cvt_pk_bf16_f32 v20, v20, s0
	v_cvt_pk_bf16_f32 v17, v17, s0
	global_store_short v[2:3], v1, off
	global_store_short v[2:3], v4, off offset:64
	global_store_short v[2:3], v20, off offset:128
	global_store_short v[2:3], v17, off offset:192
	v_mov_b32_e32 v1, v166
	s_nop 0
	v_mov_b32_e32 v2, v167
	v_mov_b32_e32 v3, v168
	v_mov_b32_e32 v4, v169
	v_rcp_f32_e32 v17, v73
	v_lshlrev_b32_e32 v1, 16, v1
	v_mul_f32_e32 v18, v21, v17
	v_lshlrev_b32_e32 v2, 16, v2
	v_mul_f32_e32 v5, v5, v17
	v_fma_f32 v18, -s78, v18, v2
	v_mul_f32_e32 v19, v37, v17
	v_lshlrev_b32_e32 v3, 16, v3
	v_fma_f32 v1, -s78, v5, v1
	v_mul_f32_e32 v2, v18, v18
	v_mul_f32_e32 v17, v53, v17
	v_lshlrev_b32_e32 v4, 16, v4
	v_fma_f32 v19, -s78, v19, v3
	v_fmac_f32_e32 v2, v1, v1
	v_fma_f32 v17, -s78, v17, v4
	v_fmac_f32_e32 v2, v19, v19
	v_fmac_f32_e32 v2, v17, v17
	ds_swizzle_b32 v3, v2 offset:swizzle(SWAP,1)
	v_mov_b32_e32 v5, v161
	s_waitcnt lgkmcnt(0)
	v_add_f32_e32 v2, v2, v3
	ds_swizzle_b32 v3, v2 offset:swizzle(SWAP,2)
	s_waitcnt lgkmcnt(0)
	v_add_f32_e32 v2, v2, v3
	ds_swizzle_b32 v3, v2 offset:swizzle(SWAP,4)
	s_waitcnt lgkmcnt(0)
	v_add_f32_e32 v2, v2, v3
	ds_swizzle_b32 v3, v2 offset:swizzle(SWAP,8)
	s_waitcnt lgkmcnt(0)
	v_add_f32_e32 v4, v2, v3
	ds_swizzle_b32 v20, v4 offset:swizzle(SWAP,16)
	v_mov_b32_e32 v2, 0xd000
	v_mov_b32_e32 v3, v161
	v_mad_u32_u24 v2, v0, s76, v2
	v_lshl_add_u64 v[2:3], v[80:81], 0, v[2:3]
	s_waitcnt lgkmcnt(0)
	v_add_f32_e32 v4, v4, v20
	v_fmamk_f32 v4, v4, 0x3c000000, v240
	v_rsq_f32_e32 v20, v4
	v_or_b32_e32 v4, 0x5000, v160
	v_lshl_add_u64 v[4:5], v[82:83], 0, v[4:5]
	v_mul_f32_e32 v1, v1, v20
	v_mul_f32_e32 v18, v18, v20
	v_mul_f32_e32 v19, v19, v20
	v_mul_f32_e32 v17, v17, v20
	v_mul_f32_e32 v1, v16, v1
	v_mul_f32_e32 v18, v32, v18
	v_mul_f32_e32 v19, v48, v19
	v_mul_f32_e32 v17, v76, v17
	v_cvt_pk_bf16_f32 v1, v1, s0
	v_cvt_pk_bf16_f32 v18, v18, s0
	v_cvt_pk_bf16_f32 v19, v19, s0
	v_cvt_pk_bf16_f32 v17, v17, s0
	global_store_short v[2:3], v1, off
	global_store_short v[2:3], v18, off offset:64
	global_store_short v[2:3], v19, off offset:128
	global_store_short v[2:3], v17, off offset:192
	v_mov_b32_e32 v1, v170
	s_nop 0
	v_mov_b32_e32 v2, v171
	v_mov_b32_e32 v3, v172
	s_nop 0
	v_mov_b32_e32 v4, v173
	v_rcp_f32_e32 v5, v74
	v_lshlrev_b32_e32 v1, 16, v1
	v_mul_f32_e32 v6, v6, v5
	v_mul_f32_e32 v17, v22, v5
	v_lshlrev_b32_e32 v2, 16, v2
	v_fma_f32 v1, -s78, v6, v1
	v_fma_f32 v6, -s78, v17, v2
	v_mul_f32_e32 v18, v38, v5
	v_lshlrev_b32_e32 v3, 16, v3
	v_mul_f32_e32 v2, v6, v6
	v_mul_f32_e32 v5, v54, v5
	v_lshlrev_b32_e32 v4, 16, v4
	v_fma_f32 v17, -s78, v18, v3
	v_fmac_f32_e32 v2, v1, v1
	v_fma_f32 v18, -s78, v5, v4
	v_fmac_f32_e32 v2, v17, v17
	v_fmac_f32_e32 v2, v18, v18
	ds_swizzle_b32 v3, v2 offset:swizzle(SWAP,1)
	v_mov_b32_e32 v5, v161
	s_waitcnt lgkmcnt(0)
	v_add_f32_e32 v2, v2, v3
	ds_swizzle_b32 v3, v2 offset:swizzle(SWAP,2)
	s_waitcnt lgkmcnt(0)
	v_add_f32_e32 v2, v2, v3
	ds_swizzle_b32 v3, v2 offset:swizzle(SWAP,4)
	s_waitcnt lgkmcnt(0)
	v_add_f32_e32 v2, v2, v3
	ds_swizzle_b32 v3, v2 offset:swizzle(SWAP,8)
	s_waitcnt lgkmcnt(0)
	v_add_f32_e32 v4, v2, v3
	ds_swizzle_b32 v19, v4 offset:swizzle(SWAP,16)
	v_mov_b32_e32 v2, 0xea00
	v_mov_b32_e32 v3, v161
	v_mad_u32_u24 v2, v0, s76, v2
	v_lshl_add_u64 v[2:3], v[80:81], 0, v[2:3]
	s_waitcnt lgkmcnt(0)
	v_add_f32_e32 v4, v4, v19
	v_fmamk_f32 v4, v4, 0x3c000000, v240
	v_rsq_f32_e32 v19, v4
	v_or_b32_e32 v4, 0x5800, v160
	v_lshl_add_u64 v[4:5], v[82:83], 0, v[4:5]
	v_mul_f32_e32 v1, v1, v19
	v_mul_f32_e32 v6, v6, v19
	v_mul_f32_e32 v17, v17, v19
	v_mul_f32_e32 v18, v18, v19
	v_mul_f32_e32 v1, v16, v1
	v_mul_f32_e32 v6, v32, v6
	v_mul_f32_e32 v17, v48, v17
	v_mul_f32_e32 v18, v76, v18
	v_cvt_pk_bf16_f32 v1, v1, s0
	v_cvt_pk_bf16_f32 v6, v6, s0
	v_cvt_pk_bf16_f32 v17, v17, s0
	v_cvt_pk_bf16_f32 v18, v18, s0
	global_store_short v[2:3], v1, off
	global_store_short v[2:3], v6, off offset:64
	global_store_short v[2:3], v17, off offset:128
	global_store_short v[2:3], v18, off offset:192
	v_mov_b32_e32 v1, v174
	s_nop 0
	v_mov_b32_e32 v2, v175
	v_mov_b32_e32 v3, v176
	s_nop 0
	v_mov_b32_e32 v4, v177
	v_rcp_f32_e32 v5, v75
	v_lshlrev_b32_e32 v1, 16, v1
	v_mul_f32_e32 v6, v7, v5
	v_mul_f32_e32 v7, v23, v5
	v_lshlrev_b32_e32 v2, 16, v2
	v_fma_f32 v1, -s78, v6, v1
	v_fma_f32 v6, -s78, v7, v2
	v_mul_f32_e32 v17, v39, v5
	v_lshlrev_b32_e32 v3, 16, v3
	v_mul_f32_e32 v2, v6, v6
	v_mul_f32_e32 v5, v55, v5
	v_lshlrev_b32_e32 v4, 16, v4
	v_fma_f32 v7, -s78, v17, v3
	v_fmac_f32_e32 v2, v1, v1
	v_fma_f32 v17, -s78, v5, v4
	v_fmac_f32_e32 v2, v7, v7
	v_fmac_f32_e32 v2, v17, v17
	ds_swizzle_b32 v3, v2 offset:swizzle(SWAP,1)
	v_mov_b32_e32 v5, v161
	s_waitcnt lgkmcnt(0)
	v_add_f32_e32 v2, v2, v3
	ds_swizzle_b32 v3, v2 offset:swizzle(SWAP,2)
	s_waitcnt lgkmcnt(0)
	v_add_f32_e32 v2, v2, v3
	ds_swizzle_b32 v3, v2 offset:swizzle(SWAP,4)
	s_waitcnt lgkmcnt(0)
	v_add_f32_e32 v2, v2, v3
	ds_swizzle_b32 v3, v2 offset:swizzle(SWAP,8)
	s_waitcnt lgkmcnt(0)
	v_add_f32_e32 v4, v2, v3
	ds_swizzle_b32 v18, v4 offset:swizzle(SWAP,16)
	v_mov_b32_e32 v2, 0x10400
	v_mov_b32_e32 v3, v161
	v_mad_u32_u24 v2, v0, s76, v2
	v_lshl_add_u64 v[2:3], v[80:81], 0, v[2:3]
	s_waitcnt lgkmcnt(0)
	v_add_f32_e32 v4, v4, v18
	v_fmamk_f32 v4, v4, 0x3c000000, v240
	v_rsq_f32_e32 v18, v4
	v_or_b32_e32 v4, 0x8000, v160
	v_lshl_add_u64 v[4:5], v[82:83], 0, v[4:5]
	v_mul_f32_e32 v1, v1, v18
	v_mul_f32_e32 v6, v6, v18
	v_mul_f32_e32 v7, v7, v18
	v_mul_f32_e32 v17, v17, v18
	v_mul_f32_e32 v1, v16, v1
	v_mul_f32_e32 v6, v32, v6
	v_mul_f32_e32 v7, v48, v7
	v_mul_f32_e32 v17, v76, v17
	v_cvt_pk_bf16_f32 v1, v1, s0
	v_cvt_pk_bf16_f32 v6, v6, s0
	v_cvt_pk_bf16_f32 v7, v7, s0
	v_cvt_pk_bf16_f32 v17, v17, s0
	global_store_short v[2:3], v1, off
	global_store_short v[2:3], v6, off offset:64
	global_store_short v[2:3], v7, off offset:128
	global_store_short v[2:3], v17, off offset:192
	v_mov_b32_e32 v1, v178
	s_nop 0
	v_mov_b32_e32 v2, v179
	v_mov_b32_e32 v3, v180
	s_nop 0
	v_mov_b32_e32 v4, v181
	v_rcp_f32_e32 v5, v68
	v_lshlrev_b32_e32 v1, 16, v1
	v_mul_f32_e32 v6, v8, v5
	v_mul_f32_e32 v7, v24, v5
	v_lshlrev_b32_e32 v2, 16, v2
	v_fma_f32 v1, -s78, v6, v1
	v_fma_f32 v6, -s78, v7, v2
	v_mul_f32_e32 v8, v40, v5
	v_lshlrev_b32_e32 v3, 16, v3
	v_mul_f32_e32 v2, v6, v6
	v_mul_f32_e32 v5, v56, v5
	v_lshlrev_b32_e32 v4, 16, v4
	v_fma_f32 v7, -s78, v8, v3
	v_fmac_f32_e32 v2, v1, v1
	v_fma_f32 v8, -s78, v5, v4
	v_fmac_f32_e32 v2, v7, v7
	v_fmac_f32_e32 v2, v8, v8
	ds_swizzle_b32 v3, v2 offset:swizzle(SWAP,1)
	v_mov_b32_e32 v5, v161
	s_waitcnt lgkmcnt(0)
	v_add_f32_e32 v2, v2, v3
	ds_swizzle_b32 v3, v2 offset:swizzle(SWAP,2)
	s_waitcnt lgkmcnt(0)
	v_add_f32_e32 v2, v2, v3
	ds_swizzle_b32 v3, v2 offset:swizzle(SWAP,4)
	s_waitcnt lgkmcnt(0)
	v_add_f32_e32 v2, v2, v3
	ds_swizzle_b32 v3, v2 offset:swizzle(SWAP,8)
	s_waitcnt lgkmcnt(0)
	v_add_f32_e32 v4, v2, v3
	ds_swizzle_b32 v17, v4 offset:swizzle(SWAP,16)
	v_mov_b32_e32 v2, 0x18600
	v_mov_b32_e32 v3, v161
	v_mad_u32_u24 v2, v0, s76, v2
	v_lshl_add_u64 v[2:3], v[80:81], 0, v[2:3]
	s_waitcnt lgkmcnt(0)
	v_add_f32_e32 v4, v4, v17
	v_fmamk_f32 v4, v4, 0x3c000000, v240
	v_rsq_f32_e32 v17, v4
	v_or_b32_e32 v4, 0x8800, v160
	v_lshl_add_u64 v[4:5], v[82:83], 0, v[4:5]
	v_mul_f32_e32 v1, v1, v17
	v_mul_f32_e32 v6, v6, v17
	v_mul_f32_e32 v7, v7, v17
	v_mul_f32_e32 v8, v8, v17
	v_mul_f32_e32 v1, v16, v1
	v_mul_f32_e32 v6, v32, v6
	v_mul_f32_e32 v7, v48, v7
	v_mul_f32_e32 v8, v76, v8
	v_cvt_pk_bf16_f32 v1, v1, s0
	v_cvt_pk_bf16_f32 v6, v6, s0
	v_cvt_pk_bf16_f32 v7, v7, s0
	v_cvt_pk_bf16_f32 v8, v8, s0
	global_store_short v[2:3], v1, off
	global_store_short v[2:3], v6, off offset:64
	global_store_short v[2:3], v7, off offset:128
	global_store_short v[2:3], v8, off offset:192
	v_mov_b32_e32 v1, v182
	s_nop 0
	v_mov_b32_e32 v2, v183
	v_mov_b32_e32 v3, v184
	s_nop 0
	v_mov_b32_e32 v4, v185
	v_rcp_f32_e32 v5, v69
	v_lshlrev_b32_e32 v1, 16, v1
	v_mul_f32_e32 v6, v9, v5
	v_mul_f32_e32 v7, v25, v5
	v_lshlrev_b32_e32 v2, 16, v2
	v_fma_f32 v1, -s78, v6, v1
	v_fma_f32 v6, -s78, v7, v2
	v_mul_f32_e32 v8, v41, v5
	v_lshlrev_b32_e32 v3, 16, v3
	v_mul_f32_e32 v2, v6, v6
	v_mul_f32_e32 v5, v57, v5
	v_lshlrev_b32_e32 v4, 16, v4
	v_fma_f32 v7, -s78, v8, v3
	v_fmac_f32_e32 v2, v1, v1
	v_fma_f32 v8, -s78, v5, v4
	v_fmac_f32_e32 v2, v7, v7
	v_fmac_f32_e32 v2, v8, v8
	ds_swizzle_b32 v3, v2 offset:swizzle(SWAP,1)
	v_mov_b32_e32 v5, v161
	s_waitcnt lgkmcnt(0)
	v_add_f32_e32 v2, v2, v3
	ds_swizzle_b32 v3, v2 offset:swizzle(SWAP,2)
	s_waitcnt lgkmcnt(0)
	v_add_f32_e32 v2, v2, v3
	ds_swizzle_b32 v3, v2 offset:swizzle(SWAP,4)
	s_waitcnt lgkmcnt(0)
	v_add_f32_e32 v2, v2, v3
	ds_swizzle_b32 v3, v2 offset:swizzle(SWAP,8)
	s_waitcnt lgkmcnt(0)
	v_add_f32_e32 v4, v2, v3
	ds_swizzle_b32 v9, v4 offset:swizzle(SWAP,16)
	v_mov_b32_e32 v2, 0x1a000
	v_mov_b32_e32 v3, v161
	v_mad_u32_u24 v2, v0, s76, v2
	v_lshl_add_u64 v[2:3], v[80:81], 0, v[2:3]
	s_waitcnt lgkmcnt(0)
	v_add_f32_e32 v4, v4, v9
	v_fmamk_f32 v4, v4, 0x3c000000, v240
	v_rsq_f32_e32 v9, v4
	v_or_b32_e32 v4, 0x9000, v160
	v_lshl_add_u64 v[4:5], v[82:83], 0, v[4:5]
	v_mul_f32_e32 v1, v1, v9
	v_mul_f32_e32 v6, v6, v9
	v_mul_f32_e32 v7, v7, v9
	v_mul_f32_e32 v8, v8, v9
	v_mul_f32_e32 v1, v16, v1
	v_mul_f32_e32 v6, v32, v6
	v_mul_f32_e32 v7, v48, v7
	v_mul_f32_e32 v8, v76, v8
	v_cvt_pk_bf16_f32 v1, v1, s0
	v_cvt_pk_bf16_f32 v6, v6, s0
	v_cvt_pk_bf16_f32 v7, v7, s0
	v_cvt_pk_bf16_f32 v8, v8, s0
	global_store_short v[2:3], v1, off
	global_store_short v[2:3], v6, off offset:64
	global_store_short v[2:3], v7, off offset:128
	global_store_short v[2:3], v8, off offset:192
	v_mov_b32_e32 v1, v186
	s_nop 0
	v_mov_b32_e32 v2, v187
	v_mov_b32_e32 v3, v188
	s_nop 0
	v_mov_b32_e32 v4, v189
	v_rcp_f32_e32 v5, v70
	v_lshlrev_b32_e32 v1, 16, v1
	v_mul_f32_e32 v6, v10, v5
	v_mul_f32_e32 v7, v26, v5
	v_lshlrev_b32_e32 v2, 16, v2
	v_fma_f32 v1, -s78, v6, v1
	v_fma_f32 v6, -s78, v7, v2
	v_mul_f32_e32 v8, v42, v5
	v_lshlrev_b32_e32 v3, 16, v3
	v_mul_f32_e32 v2, v6, v6
	v_mul_f32_e32 v5, v58, v5
	v_lshlrev_b32_e32 v4, 16, v4
	v_fma_f32 v7, -s78, v8, v3
	v_fmac_f32_e32 v2, v1, v1
	v_fma_f32 v8, -s78, v5, v4
	v_fmac_f32_e32 v2, v7, v7
	v_fmac_f32_e32 v2, v8, v8
	ds_swizzle_b32 v3, v2 offset:swizzle(SWAP,1)
	v_mov_b32_e32 v5, v161
	s_waitcnt lgkmcnt(0)
	v_add_f32_e32 v2, v2, v3
	ds_swizzle_b32 v3, v2 offset:swizzle(SWAP,2)
	s_waitcnt lgkmcnt(0)
	v_add_f32_e32 v2, v2, v3
	ds_swizzle_b32 v3, v2 offset:swizzle(SWAP,4)
	s_waitcnt lgkmcnt(0)
	v_add_f32_e32 v2, v2, v3
	ds_swizzle_b32 v3, v2 offset:swizzle(SWAP,8)
	s_waitcnt lgkmcnt(0)
	v_add_f32_e32 v4, v2, v3
	ds_swizzle_b32 v9, v4 offset:swizzle(SWAP,16)
	v_mov_b32_e32 v2, 0x1ba00
	v_mov_b32_e32 v3, v161
	v_mad_u32_u24 v2, v0, s76, v2
	v_lshl_add_u64 v[2:3], v[80:81], 0, v[2:3]
	s_waitcnt lgkmcnt(0)
	v_add_f32_e32 v4, v4, v9
	v_fmamk_f32 v4, v4, 0x3c000000, v240
	v_rsq_f32_e32 v9, v4
	v_or_b32_e32 v4, 0x9800, v160
	v_lshl_add_u64 v[4:5], v[82:83], 0, v[4:5]
	v_mul_f32_e32 v1, v1, v9
	v_mul_f32_e32 v6, v6, v9
	v_mul_f32_e32 v7, v7, v9
	v_mul_f32_e32 v8, v8, v9
	v_mul_f32_e32 v1, v16, v1
	v_mul_f32_e32 v6, v32, v6
	v_mul_f32_e32 v7, v48, v7
	v_mul_f32_e32 v8, v76, v8
	v_cvt_pk_bf16_f32 v1, v1, s0
	v_cvt_pk_bf16_f32 v6, v6, s0
	v_cvt_pk_bf16_f32 v7, v7, s0
	v_cvt_pk_bf16_f32 v8, v8, s0
	global_store_short v[2:3], v1, off
	global_store_short v[2:3], v6, off offset:64
	global_store_short v[2:3], v7, off offset:128
	global_store_short v[2:3], v8, off offset:192
	v_mov_b32_e32 v1, v191
	s_nop 0
	v_mov_b32_e32 v2, v192
	v_mov_b32_e32 v3, v193
	s_nop 0
	v_mov_b32_e32 v4, v194
	v_rcp_f32_e32 v5, v71
	v_lshlrev_b32_e32 v1, 16, v1
	v_mul_f32_e32 v6, v11, v5
	v_mul_f32_e32 v7, v27, v5
	v_lshlrev_b32_e32 v2, 16, v2
	v_fma_f32 v1, -s78, v6, v1
	v_fma_f32 v6, -s78, v7, v2
	v_mul_f32_e32 v8, v43, v5
	v_lshlrev_b32_e32 v3, 16, v3
	v_mul_f32_e32 v2, v6, v6
	v_mul_f32_e32 v5, v59, v5
	v_lshlrev_b32_e32 v4, 16, v4
	v_fma_f32 v7, -s78, v8, v3
	v_fmac_f32_e32 v2, v1, v1
	v_fma_f32 v8, -s78, v5, v4
	v_fmac_f32_e32 v2, v7, v7
	v_fmac_f32_e32 v2, v8, v8
	ds_swizzle_b32 v3, v2 offset:swizzle(SWAP,1)
	v_mov_b32_e32 v5, v161
	s_waitcnt lgkmcnt(0)
	v_add_f32_e32 v2, v2, v3
	ds_swizzle_b32 v3, v2 offset:swizzle(SWAP,2)
	s_waitcnt lgkmcnt(0)
	v_add_f32_e32 v2, v2, v3
	ds_swizzle_b32 v3, v2 offset:swizzle(SWAP,4)
	s_waitcnt lgkmcnt(0)
	v_add_f32_e32 v2, v2, v3
	ds_swizzle_b32 v3, v2 offset:swizzle(SWAP,8)
	s_waitcnt lgkmcnt(0)
	v_add_f32_e32 v4, v2, v3
	ds_swizzle_b32 v9, v4 offset:swizzle(SWAP,16)
	v_mov_b32_e32 v2, 0x1d400
	v_mov_b32_e32 v3, v161
	v_mad_u32_u24 v2, v0, s76, v2
	v_lshl_add_u64 v[2:3], v[80:81], 0, v[2:3]
	s_waitcnt lgkmcnt(0)
	v_add_f32_e32 v4, v4, v9
	v_fmamk_f32 v4, v4, 0x3c000000, v240
	v_rsq_f32_e32 v9, v4
	v_or_b32_e32 v4, 0xc000, v160
	v_lshl_add_u64 v[4:5], v[82:83], 0, v[4:5]
	v_mul_f32_e32 v1, v1, v9
	v_mul_f32_e32 v6, v6, v9
	v_mul_f32_e32 v7, v7, v9
	v_mul_f32_e32 v8, v8, v9
	v_mul_f32_e32 v1, v16, v1
	v_mul_f32_e32 v6, v32, v6
	v_mul_f32_e32 v7, v48, v7
	v_mul_f32_e32 v8, v76, v8
	v_cvt_pk_bf16_f32 v1, v1, s0
	v_cvt_pk_bf16_f32 v6, v6, s0
	v_cvt_pk_bf16_f32 v7, v7, s0
	v_cvt_pk_bf16_f32 v8, v8, s0
	global_store_short v[2:3], v1, off
	global_store_short v[2:3], v6, off offset:64
	global_store_short v[2:3], v7, off offset:128
	global_store_short v[2:3], v8, off offset:192
	v_mov_b32_e32 v1, v195
	s_nop 0
	v_mov_b32_e32 v2, v196
	v_mov_b32_e32 v3, v197
	s_nop 0
	v_mov_b32_e32 v4, v198
	v_rcp_f32_e32 v5, v64
	v_lshlrev_b32_e32 v1, 16, v1
	v_mul_f32_e32 v6, v12, v5
	v_mul_f32_e32 v7, v28, v5
	v_lshlrev_b32_e32 v2, 16, v2
	v_fma_f32 v1, -s78, v6, v1
	v_fma_f32 v6, -s78, v7, v2
	v_mul_f32_e32 v8, v44, v5
	v_lshlrev_b32_e32 v3, 16, v3
	v_mul_f32_e32 v2, v6, v6
	v_mul_f32_e32 v5, v60, v5
	v_lshlrev_b32_e32 v4, 16, v4
	v_fma_f32 v7, -s78, v8, v3
	v_fmac_f32_e32 v2, v1, v1
	v_fma_f32 v8, -s78, v5, v4
	v_fmac_f32_e32 v2, v7, v7
	v_fmac_f32_e32 v2, v8, v8
	ds_swizzle_b32 v3, v2 offset:swizzle(SWAP,1)
	v_mov_b32_e32 v5, v161
	s_waitcnt lgkmcnt(0)
	v_add_f32_e32 v2, v2, v3
	ds_swizzle_b32 v3, v2 offset:swizzle(SWAP,2)
	s_waitcnt lgkmcnt(0)
	v_add_f32_e32 v2, v2, v3
	ds_swizzle_b32 v3, v2 offset:swizzle(SWAP,4)
	s_waitcnt lgkmcnt(0)
	v_add_f32_e32 v2, v2, v3
	ds_swizzle_b32 v3, v2 offset:swizzle(SWAP,8)
	s_waitcnt lgkmcnt(0)
	v_add_f32_e32 v4, v2, v3
	ds_swizzle_b32 v9, v4 offset:swizzle(SWAP,16)
	v_mov_b32_e32 v2, 0x25600
	v_mov_b32_e32 v3, v161
	v_mad_u32_u24 v2, v0, s76, v2
	v_lshl_add_u64 v[2:3], v[80:81], 0, v[2:3]
	s_waitcnt lgkmcnt(0)
	v_add_f32_e32 v4, v4, v9
	v_fmamk_f32 v4, v4, 0x3c000000, v240
	v_rsq_f32_e32 v9, v4
	v_or_b32_e32 v4, 0xc800, v160
	v_lshl_add_u64 v[4:5], v[82:83], 0, v[4:5]
	v_mul_f32_e32 v1, v1, v9
	v_mul_f32_e32 v6, v6, v9
	v_mul_f32_e32 v7, v7, v9
	v_mul_f32_e32 v8, v8, v9
	v_mul_f32_e32 v1, v16, v1
	v_mul_f32_e32 v6, v32, v6
	v_mul_f32_e32 v7, v48, v7
	v_mul_f32_e32 v8, v76, v8
	v_cvt_pk_bf16_f32 v1, v1, s0
	v_cvt_pk_bf16_f32 v6, v6, s0
	v_cvt_pk_bf16_f32 v7, v7, s0
	v_cvt_pk_bf16_f32 v8, v8, s0
	global_store_short v[2:3], v1, off
	global_store_short v[2:3], v6, off offset:64
	global_store_short v[2:3], v7, off offset:128
	global_store_short v[2:3], v8, off offset:192
	v_mov_b32_e32 v1, v199
	s_nop 0
	v_mov_b32_e32 v2, v200
	v_mov_b32_e32 v3, v201
	s_nop 0
	v_mov_b32_e32 v4, v205
	v_rcp_f32_e32 v5, v65
	v_lshlrev_b32_e32 v1, 16, v1
	v_mul_f32_e32 v6, v13, v5
	v_mul_f32_e32 v7, v29, v5
	v_lshlrev_b32_e32 v2, 16, v2
	v_fma_f32 v1, -s78, v6, v1
	v_fma_f32 v6, -s78, v7, v2
	v_mul_f32_e32 v8, v45, v5
	v_lshlrev_b32_e32 v3, 16, v3
	v_mul_f32_e32 v2, v6, v6
	v_mul_f32_e32 v5, v61, v5
	v_lshlrev_b32_e32 v4, 16, v4
	v_fma_f32 v7, -s78, v8, v3
	v_fmac_f32_e32 v2, v1, v1
	v_fma_f32 v8, -s78, v5, v4
	v_fmac_f32_e32 v2, v7, v7
	v_fmac_f32_e32 v2, v8, v8
	ds_swizzle_b32 v3, v2 offset:swizzle(SWAP,1)
	v_mov_b32_e32 v5, v161
	s_waitcnt lgkmcnt(0)
	v_add_f32_e32 v2, v2, v3
	ds_swizzle_b32 v3, v2 offset:swizzle(SWAP,2)
	s_waitcnt lgkmcnt(0)
	v_add_f32_e32 v2, v2, v3
	ds_swizzle_b32 v3, v2 offset:swizzle(SWAP,4)
	s_waitcnt lgkmcnt(0)
	v_add_f32_e32 v2, v2, v3
	ds_swizzle_b32 v3, v2 offset:swizzle(SWAP,8)
	s_waitcnt lgkmcnt(0)
	v_add_f32_e32 v4, v2, v3
	ds_swizzle_b32 v9, v4 offset:swizzle(SWAP,16)
	v_mov_b32_e32 v2, 0x27000
	v_mov_b32_e32 v3, v161
	v_mad_u32_u24 v2, v0, s76, v2
	v_lshl_add_u64 v[2:3], v[80:81], 0, v[2:3]
	s_waitcnt lgkmcnt(0)
	v_add_f32_e32 v4, v4, v9
	v_fmamk_f32 v4, v4, 0x3c000000, v240
	v_rsq_f32_e32 v9, v4
	v_or_b32_e32 v4, 0xd000, v160
	v_lshl_add_u64 v[4:5], v[82:83], 0, v[4:5]
	v_or_b32_e32 v160, 0xd800, v160
	v_mul_f32_e32 v1, v1, v9
	v_mul_f32_e32 v6, v6, v9
	v_mul_f32_e32 v7, v7, v9
	v_mul_f32_e32 v8, v8, v9
	v_mul_f32_e32 v1, v16, v1
	v_mul_f32_e32 v6, v32, v6
	v_mul_f32_e32 v7, v48, v7
	v_mul_f32_e32 v8, v76, v8
	v_cvt_pk_bf16_f32 v1, v1, s0
	v_cvt_pk_bf16_f32 v6, v6, s0
	v_cvt_pk_bf16_f32 v7, v7, s0
	v_cvt_pk_bf16_f32 v8, v8, s0
	global_store_short v[2:3], v1, off
	global_store_short v[2:3], v6, off offset:64
	global_store_short v[2:3], v7, off offset:128
	global_store_short v[2:3], v8, off offset:192
	v_mov_b32_e32 v1, v206
	s_nop 0
	v_mov_b32_e32 v2, v207
	v_mov_b32_e32 v3, v208
	s_nop 0
	v_mov_b32_e32 v4, v209
	v_rcp_f32_e32 v5, v66
	v_lshlrev_b32_e32 v1, 16, v1
	v_mul_f32_e32 v6, v14, v5
	v_mul_f32_e32 v7, v30, v5
	v_lshlrev_b32_e32 v2, 16, v2
	v_fma_f32 v1, -s78, v6, v1
	v_fma_f32 v6, -s78, v7, v2
	v_mul_f32_e32 v8, v46, v5
	v_lshlrev_b32_e32 v3, 16, v3
	v_mul_f32_e32 v2, v6, v6
	v_mul_f32_e32 v5, v62, v5
	v_lshlrev_b32_e32 v4, 16, v4
	v_fma_f32 v7, -s78, v8, v3
	v_fmac_f32_e32 v2, v1, v1
	v_fma_f32 v8, -s78, v5, v4
	v_fmac_f32_e32 v2, v7, v7
	v_fmac_f32_e32 v2, v8, v8
	ds_swizzle_b32 v3, v2 offset:swizzle(SWAP,1)
	s_waitcnt lgkmcnt(0)
	v_add_f32_e32 v2, v2, v3
	ds_swizzle_b32 v3, v2 offset:swizzle(SWAP,2)
	s_waitcnt lgkmcnt(0)
	v_add_f32_e32 v2, v2, v3
	ds_swizzle_b32 v3, v2 offset:swizzle(SWAP,4)
	s_waitcnt lgkmcnt(0)
	v_add_f32_e32 v2, v2, v3
	ds_swizzle_b32 v3, v2 offset:swizzle(SWAP,8)
	s_waitcnt lgkmcnt(0)
	v_add_f32_e32 v4, v2, v3
	ds_swizzle_b32 v5, v4 offset:swizzle(SWAP,16)
	v_mov_b32_e32 v2, 0x28a00
	v_mov_b32_e32 v3, v161
	v_mad_u32_u24 v2, v0, s76, v2
	v_lshl_add_u64 v[2:3], v[80:81], 0, v[2:3]
	s_waitcnt lgkmcnt(0)
	v_add_f32_e32 v4, v4, v5
	v_fmamk_f32 v4, v4, 0x3c000000, v240
	v_rsq_f32_e32 v9, v4
	v_lshl_add_u64 v[4:5], v[82:83], 0, v[160:161]
	v_mul_f32_e32 v1, v1, v9
	v_mul_f32_e32 v6, v6, v9
	v_mul_f32_e32 v7, v7, v9
	v_mul_f32_e32 v8, v8, v9
	v_mul_f32_e32 v1, v16, v1
	v_mul_f32_e32 v6, v32, v6
	v_mul_f32_e32 v7, v48, v7
	v_mul_f32_e32 v8, v76, v8
	v_cvt_pk_bf16_f32 v1, v1, s0
	v_cvt_pk_bf16_f32 v6, v6, s0
	v_cvt_pk_bf16_f32 v7, v7, s0
	v_cvt_pk_bf16_f32 v8, v8, s0
	global_store_short v[2:3], v1, off
	global_store_short v[2:3], v6, off offset:64
	global_store_short v[2:3], v7, off offset:128
	global_store_short v[2:3], v8, off offset:192
	v_mov_b32_e32 v1, v210
	s_nop 0
	v_mov_b32_e32 v2, v211
	v_mov_b32_e32 v3, v212
	s_nop 0
	v_mov_b32_e32 v4, v213
	v_rcp_f32_e32 v5, v67
	v_lshlrev_b32_e32 v1, 16, v1
	v_mul_f32_e32 v7, v31, v5
	v_lshlrev_b32_e32 v2, 16, v2
	v_mul_f32_e32 v6, v15, v5
	v_fma_f32 v2, -s78, v7, v2
	v_mul_f32_e32 v8, v47, v5
	v_lshlrev_b32_e32 v3, 16, v3
	v_fma_f32 v6, -s78, v6, v1
	v_mul_f32_e32 v1, v2, v2
	v_mul_f32_e32 v5, v63, v5
	v_lshlrev_b32_e32 v4, 16, v4
	v_fma_f32 v3, -s78, v8, v3
	v_fmac_f32_e32 v1, v6, v6
	v_fma_f32 v4, -s78, v5, v4
	v_fmac_f32_e32 v1, v3, v3
	v_fmac_f32_e32 v1, v4, v4
	ds_swizzle_b32 v5, v1 offset:swizzle(SWAP,1)
	s_waitcnt lgkmcnt(0)
	v_add_f32_e32 v1, v1, v5
	ds_swizzle_b32 v5, v1 offset:swizzle(SWAP,2)
	s_waitcnt lgkmcnt(0)
	v_add_f32_e32 v1, v1, v5
	ds_swizzle_b32 v5, v1 offset:swizzle(SWAP,4)
	s_waitcnt lgkmcnt(0)
	v_add_f32_e32 v1, v1, v5
	ds_swizzle_b32 v5, v1 offset:swizzle(SWAP,8)
	s_waitcnt lgkmcnt(0)
	v_add_f32_e32 v1, v1, v5
	ds_swizzle_b32 v5, v1 offset:swizzle(SWAP,16)
	s_waitcnt lgkmcnt(0)
	v_add_f32_e32 v1, v1, v5
	v_fmamk_f32 v1, v1, 0x3c000000, v240
	v_rsq_f32_e32 v5, v1
	v_mov_b32_e32 v1, 0x2a400
	v_mad_u32_u24 v160, v0, s76, v1
	v_lshl_add_u64 v[0:1], v[80:81], 0, v[160:161]
	v_mul_f32_e32 v6, v6, v5
	v_mul_f32_e32 v2, v2, v5
	v_mul_f32_e32 v3, v3, v5
	v_mul_f32_e32 v4, v4, v5
	v_mul_f32_e32 v5, v16, v6
	v_mul_f32_e32 v2, v32, v2
	v_mul_f32_e32 v3, v48, v3
	v_mul_f32_e32 v4, v76, v4
	v_cvt_pk_bf16_f32 v5, v5, s0
	v_cvt_pk_bf16_f32 v2, v2, s0
	v_cvt_pk_bf16_f32 v3, v3, s0
	v_cvt_pk_bf16_f32 v4, v4, s0
	global_store_short v[0:1], v5, off
	global_store_short v[0:1], v2, off offset:64
	global_store_short v[0:1], v3, off offset:128
	global_store_short v[0:1], v4, off offset:192
	s_barrier
	s_cbranch_scc1 .LBB0_596
